# speedup vs baseline: 1.0038x; 1.0011x over previous
.LBB2_8:
	s_or_b64 exec, exec, s[0:1]
	v_cmp_gt_i32_e64 s[6:7], 1, v97
	v_cmp_lt_i32_e64 s[0:1], 0, v97
	s_and_saveexec_b64 s[10:11], s[0:1]
	s_cbranch_execz .LBB2_10
	v_ashrrev_i32_e32 v7, 31, v52
	v_mov_b32_e32 v6, v52
	v_lshlrev_b64 v[6:7], 7, v[6:7]
	v_lshl_add_u64 v[6:7], v[60:61], 0, v[6:7]
	global_load_dwordx4 v[6:9], v[6:7], off nt
